# in_proj/out_proj: per-unit accumulator zeroing removed, first K iteration peeled with C=0; MoE2 header expert-id read dedup (s100)
# baseline (speedup 1.0000x reference)
.LBB0_488:
	s_ashr_i32 s21, s20, 31
	s_lshl_b64 s[24:25], s[20:21], 19
	s_add_u32 s24, s43, s24
	s_addc_u32 s25, s44, s25
	s_and_b64 s[30:31], s[30:31], exec
	s_cselect_b32 s11, s25, s29
	s_cselect_b32 s19, s24, s28
	s_add_u32 s26, s26, 0x40080
	s_addc_u32 s27, s27, 0
	s_add_u32 s21, s28, 0x100
	s_addc_u32 s49, s29, 0
	s_mov_b32 s67, -2
	s_add_u32 s28, s26, 0xfffc0080
	s_addc_u32 s29, s27, -1
	s_cmp_eq_u32 s67, 12
	s_cselect_b32 s31, s23, s29
	s_cselect_b32 s30, s22, s28
	s_cselect_b32 s29, s11, s49
	s_cselect_b32 s28, s19, s21
	s_add_i32 s55, 0, 0x10000
	s_add_i32 s70, 0, 0x14000
	v_add_u32_e32 v118, s55, v165
	v_add_u32_e32 v162, s70, v165
	ds_read_b128 v[98:101], v118
	ds_read_b128 v[102:105], v118 offset:1024
	ds_read_b128 v[114:117], v118 offset:2048
	ds_read_b128 v[118:121], v118 offset:3072
	ds_read_b128 v[158:161], v162
	ds_read_b128 v[170:173], v162 offset:1024
	ds_read_b128 v[174:177], v162 offset:2048
	ds_read_b128 v[178:181], v162 offset:3072
	v_lshl_add_u64 v[162:163], s[26:27], 0, v[154:155]
	s_add_i32 m0, s48, 0xc000
	ds_read_b128 v[182:185], v168
	ds_read_b128 v[186:189], v168 offset:1024
	ds_read_b128 v[190:193], v168 offset:2048
	ds_read_b128 v[194:197], v168 offset:3072
	ds_read_b128 v[198:201], v168 offset:4096
	ds_read_b128 v[206:209], v168 offset:5120
	ds_read_b128 v[210:213], v168 offset:6144
	ds_read_b128 v[214:217], v168 offset:7168
	global_load_lds_dwordx4 v[162:163], off
	v_lshl_add_u64 v[162:163], s[26:27], 0, v[156:157]
	s_add_i32 m0, s48, 0xe000
	s_nop 0
	global_load_lds_dwordx4 v[162:163], off
	s_waitcnt vmcnt(8)
	s_waitcnt lgkmcnt(0)
	s_barrier
	s_setprio 1
	s_waitcnt lgkmcnt(0)
	v_mfma_f32_16x16x32_bf16 v[142:145], v[98:101], v[182:185], 0
	v_mfma_f32_16x16x32_bf16 v[138:141], v[114:117], v[182:185], 0
	v_mfma_f32_16x16x32_bf16 v[126:129], v[98:101], v[190:193], 0
	v_mfma_f32_16x16x32_bf16 v[122:125], v[114:117], v[190:193], 0
	v_mfma_f32_16x16x32_bf16 v[94:97], v[98:101], v[198:201], 0
	v_mfma_f32_16x16x32_bf16 v[90:93], v[114:117], v[198:201], 0
	v_mfma_f32_16x16x32_bf16 v[78:81], v[98:101], v[210:213], 0
	v_mfma_f32_16x16x32_bf16 v[74:77], v[114:117], v[210:213], 0
	v_mfma_f32_16x16x32_bf16 v[142:145], v[102:105], v[186:189], v[142:145]
	v_mfma_f32_16x16x32_bf16 v[138:141], v[118:121], v[186:189], v[138:141]
	v_mfma_f32_16x16x32_bf16 v[126:129], v[102:105], v[194:197], v[126:129]
	v_mfma_f32_16x16x32_bf16 v[122:125], v[118:121], v[194:197], v[122:125]
	v_mfma_f32_16x16x32_bf16 v[94:97], v[102:105], v[206:209], v[94:97]
	v_mfma_f32_16x16x32_bf16 v[90:93], v[118:121], v[206:209], v[90:93]
	v_mfma_f32_16x16x32_bf16 v[78:81], v[102:105], v[214:217], v[78:81]
	v_mfma_f32_16x16x32_bf16 v[74:77], v[118:121], v[214:217], v[74:77]
	s_setprio 0
	s_setprio 1
	v_mfma_f32_16x16x32_bf16 v[134:137], v[158:161], v[182:185], 0
	v_mfma_f32_16x16x32_bf16 v[130:133], v[174:177], v[182:185], 0
	v_mfma_f32_16x16x32_bf16 v[110:113], v[158:161], v[190:193], 0
	v_mfma_f32_16x16x32_bf16 v[106:109], v[174:177], v[190:193], 0
	v_mfma_f32_16x16x32_bf16 v[86:89], v[158:161], v[198:201], 0
	v_mfma_f32_16x16x32_bf16 v[82:85], v[174:177], v[198:201], 0
	v_mfma_f32_16x16x32_bf16 v[70:73], v[158:161], v[210:213], 0
	v_mfma_f32_16x16x32_bf16 v[66:69], v[174:177], v[210:213], 0
	v_mfma_f32_16x16x32_bf16 v[134:137], v[170:173], v[186:189], v[134:137]
	v_mfma_f32_16x16x32_bf16 v[130:133], v[178:181], v[186:189], v[130:133]
	v_mfma_f32_16x16x32_bf16 v[110:113], v[170:173], v[194:197], v[110:113]
	v_mfma_f32_16x16x32_bf16 v[106:109], v[178:181], v[194:197], v[106:109]
	v_mfma_f32_16x16x32_bf16 v[86:89], v[170:173], v[206:209], v[86:89]
	v_mfma_f32_16x16x32_bf16 v[82:85], v[178:181], v[206:209], v[82:85]
	v_mfma_f32_16x16x32_bf16 v[70:73], v[170:173], v[214:217], v[70:73]
	v_mfma_f32_16x16x32_bf16 v[66:69], v[178:181], v[214:217], v[66:69]
	s_setprio 0
	s_barrier
	s_add_i32 s55, s55, s40
	v_lshl_add_u64 v[162:163], s[28:29], 0, v[0:1]
	s_mov_b32 m0, s55
	ds_read_b128 v[182:185], v168 offset:16384
	ds_read_b128 v[186:189], v168 offset:17408
	ds_read_b128 v[190:193], v168 offset:18432
	ds_read_b128 v[194:197], v168 offset:19456
	ds_read_b128 v[198:201], v168 offset:20480
	ds_read_b128 v[206:209], v168 offset:21504
	ds_read_b128 v[210:213], v168 offset:22528
	ds_read_b128 v[214:217], v168 offset:23552
	global_load_lds_dwordx4 v[162:163], off
	s_add_i32 m0, s55, 0x2000
	s_add_u32 s68, s28, 0x40000
	v_lshl_add_u64 v[202:203], s[28:29], 0, v[146:147]
	s_addc_u32 s69, s29, 0
	s_add_i32 s55, s70, s40
	global_load_lds_dwordx4 v[202:203], off
	v_lshl_add_u64 v[218:219], s[68:69], 0, v[0:1]
	s_mov_b32 m0, s55
	v_lshl_add_u64 v[222:223], s[30:31], 0, v[150:151]
	global_load_lds_dwordx4 v[218:219], off
	v_lshl_add_u64 v[218:219], s[68:69], 0, v[146:147]
	s_add_i32 m0, s55, 0x2000
	s_nop 0
	global_load_lds_dwordx4 v[218:219], off
	v_lshl_add_u64 v[218:219], s[30:31], 0, v[148:149]
	s_mov_b32 m0, s48
	s_nop 0
	global_load_lds_dwordx4 v[218:219], off
	s_mov_b32 m0, s51
	s_nop 0
	global_load_lds_dwordx4 v[222:223], off
	s_waitcnt vmcnt(8)
	s_waitcnt lgkmcnt(0)
	s_barrier
	s_setprio 1
	s_waitcnt lgkmcnt(0)
	v_mfma_f32_16x16x32_bf16 v[62:65], v[98:101], v[182:185], 0
	v_mfma_f32_16x16x32_bf16 v[58:61], v[114:117], v[182:185], 0
	v_mfma_f32_16x16x32_bf16 v[46:49], v[98:101], v[190:193], 0
	v_mfma_f32_16x16x32_bf16 v[42:45], v[114:117], v[190:193], 0
	v_mfma_f32_16x16x32_bf16 v[30:33], v[98:101], v[198:201], 0
	v_mfma_f32_16x16x32_bf16 v[26:29], v[114:117], v[198:201], 0
	v_mfma_f32_16x16x32_bf16 v[14:17], v[98:101], v[210:213], 0
	v_mfma_f32_16x16x32_bf16 v[10:13], v[114:117], v[210:213], 0
	v_mfma_f32_16x16x32_bf16 v[62:65], v[102:105], v[186:189], v[62:65]
	v_mfma_f32_16x16x32_bf16 v[58:61], v[118:121], v[186:189], v[58:61]
	v_mfma_f32_16x16x32_bf16 v[46:49], v[102:105], v[194:197], v[46:49]
	v_mfma_f32_16x16x32_bf16 v[42:45], v[118:121], v[194:197], v[42:45]
	v_mfma_f32_16x16x32_bf16 v[30:33], v[102:105], v[206:209], v[30:33]
	v_mfma_f32_16x16x32_bf16 v[26:29], v[118:121], v[206:209], v[26:29]
	v_mfma_f32_16x16x32_bf16 v[14:17], v[102:105], v[214:217], v[14:17]
	v_mfma_f32_16x16x32_bf16 v[10:13], v[118:121], v[214:217], v[10:13]
	s_setprio 0
	s_setprio 1
	v_mfma_f32_16x16x32_bf16 v[54:57], v[158:161], v[182:185], 0
	v_mfma_f32_16x16x32_bf16 v[50:53], v[174:177], v[182:185], 0
	v_mfma_f32_16x16x32_bf16 v[38:41], v[158:161], v[190:193], 0
	v_mfma_f32_16x16x32_bf16 v[34:37], v[174:177], v[190:193], 0
	v_mfma_f32_16x16x32_bf16 v[22:25], v[158:161], v[198:201], 0
	v_mfma_f32_16x16x32_bf16 v[18:21], v[174:177], v[198:201], 0
	v_mfma_f32_16x16x32_bf16 v[6:9], v[158:161], v[210:213], 0
	v_mfma_f32_16x16x32_bf16 v[2:5], v[174:177], v[210:213], 0
	v_mfma_f32_16x16x32_bf16 v[54:57], v[170:173], v[186:189], v[54:57]
	v_mfma_f32_16x16x32_bf16 v[50:53], v[178:181], v[186:189], v[50:53]
	v_mfma_f32_16x16x32_bf16 v[38:41], v[170:173], v[194:197], v[38:41]
	v_mfma_f32_16x16x32_bf16 v[34:37], v[178:181], v[194:197], v[34:37]
	v_mfma_f32_16x16x32_bf16 v[22:25], v[170:173], v[206:209], v[22:25]
	v_mfma_f32_16x16x32_bf16 v[18:21], v[178:181], v[206:209], v[18:21]
	v_mfma_f32_16x16x32_bf16 v[6:9], v[170:173], v[214:217], v[6:9]
	v_mfma_f32_16x16x32_bf16 v[2:5], v[178:181], v[214:217], v[2:5]
	s_setprio 0
	s_barrier
	s_add_i32 s55, 0, 0x18000
	s_add_i32 s68, 0, 0x1c000
	v_add_u32_e32 v118, s55, v165
	v_add_u32_e32 v169, s68, v165
	ds_read_b128 v[98:101], v118
	ds_read_b128 v[102:105], v118 offset:1024
	ds_read_b128 v[114:117], v118 offset:2048
	ds_read_b128 v[118:121], v118 offset:3072
	ds_read_b128 v[158:161], v169
	ds_read_b128 v[170:173], v169 offset:1024
	ds_read_b128 v[174:177], v169 offset:2048
	ds_read_b128 v[178:181], v169 offset:3072
	s_add_u32 s30, s30, 0x40000
	s_addc_u32 s31, s31, 0
	s_mov_b32 m0, s52
	v_lshl_add_u64 v[224:225], s[30:31], 0, v[148:149]
	ds_read_b128 v[182:185], v168 offset:32768
	ds_read_b128 v[186:189], v168 offset:33792
	ds_read_b128 v[190:193], v168 offset:34816
	ds_read_b128 v[194:197], v168 offset:35840
	ds_read_b128 v[198:201], v168 offset:36864
	ds_read_b128 v[206:209], v168 offset:37888
	ds_read_b128 v[210:213], v168 offset:38912
	ds_read_b128 v[214:217], v168 offset:39936
	global_load_lds_dwordx4 v[224:225], off
	v_lshl_add_u64 v[224:225], s[30:31], 0, v[150:151]
	s_mov_b32 m0, s53
	s_nop 0
	global_load_lds_dwordx4 v[224:225], off
	s_waitcnt vmcnt(8)
	s_waitcnt lgkmcnt(0)
	s_barrier
	s_setprio 1
	s_waitcnt lgkmcnt(0)
	v_mfma_f32_16x16x32_bf16 v[142:145], v[98:101], v[182:185], v[142:145]
	v_mfma_f32_16x16x32_bf16 v[138:141], v[114:117], v[182:185], v[138:141]
	v_mfma_f32_16x16x32_bf16 v[126:129], v[98:101], v[190:193], v[126:129]
	v_mfma_f32_16x16x32_bf16 v[122:125], v[114:117], v[190:193], v[122:125]
	v_mfma_f32_16x16x32_bf16 v[94:97], v[98:101], v[198:201], v[94:97]
	v_mfma_f32_16x16x32_bf16 v[90:93], v[114:117], v[198:201], v[90:93]
	v_mfma_f32_16x16x32_bf16 v[78:81], v[98:101], v[210:213], v[78:81]
	v_mfma_f32_16x16x32_bf16 v[74:77], v[114:117], v[210:213], v[74:77]
	v_mfma_f32_16x16x32_bf16 v[142:145], v[102:105], v[186:189], v[142:145]
	v_mfma_f32_16x16x32_bf16 v[138:141], v[118:121], v[186:189], v[138:141]
	v_mfma_f32_16x16x32_bf16 v[126:129], v[102:105], v[194:197], v[126:129]
	v_mfma_f32_16x16x32_bf16 v[122:125], v[118:121], v[194:197], v[122:125]
	v_mfma_f32_16x16x32_bf16 v[94:97], v[102:105], v[206:209], v[94:97]
	v_mfma_f32_16x16x32_bf16 v[90:93], v[118:121], v[206:209], v[90:93]
	v_mfma_f32_16x16x32_bf16 v[78:81], v[102:105], v[214:217], v[78:81]
	v_mfma_f32_16x16x32_bf16 v[74:77], v[118:121], v[214:217], v[74:77]
	s_setprio 0
	s_setprio 1
	v_mfma_f32_16x16x32_bf16 v[134:137], v[158:161], v[182:185], v[134:137]
	v_mfma_f32_16x16x32_bf16 v[130:133], v[174:177], v[182:185], v[130:133]
	v_mfma_f32_16x16x32_bf16 v[110:113], v[158:161], v[190:193], v[110:113]
	v_mfma_f32_16x16x32_bf16 v[106:109], v[174:177], v[190:193], v[106:109]
	v_mfma_f32_16x16x32_bf16 v[86:89], v[158:161], v[198:201], v[86:89]
	v_mfma_f32_16x16x32_bf16 v[82:85], v[174:177], v[198:201], v[82:85]
	v_mfma_f32_16x16x32_bf16 v[70:73], v[158:161], v[210:213], v[70:73]
	v_mfma_f32_16x16x32_bf16 v[66:69], v[174:177], v[210:213], v[66:69]
	v_mfma_f32_16x16x32_bf16 v[134:137], v[170:173], v[186:189], v[134:137]
	v_mfma_f32_16x16x32_bf16 v[130:133], v[178:181], v[186:189], v[130:133]
	v_mfma_f32_16x16x32_bf16 v[110:113], v[170:173], v[194:197], v[110:113]
	v_mfma_f32_16x16x32_bf16 v[106:109], v[178:181], v[194:197], v[106:109]
	v_mfma_f32_16x16x32_bf16 v[86:89], v[170:173], v[206:209], v[86:89]
	v_mfma_f32_16x16x32_bf16 v[82:85], v[178:181], v[206:209], v[82:85]
	v_mfma_f32_16x16x32_bf16 v[70:73], v[170:173], v[214:217], v[70:73]
	v_mfma_f32_16x16x32_bf16 v[66:69], v[178:181], v[214:217], v[66:69]
	s_setprio 0
	s_barrier
	s_add_i32 s30, s55, s40
	v_lshl_add_u64 v[162:163], v[162:163], 0, s[78:79]
	s_mov_b32 m0, s30
	ds_read_b128 v[182:185], v168 offset:49152
	ds_read_b128 v[186:189], v168 offset:50176
	ds_read_b128 v[190:193], v168 offset:51200
	ds_read_b128 v[194:197], v168 offset:52224
	ds_read_b128 v[198:201], v168 offset:53248
	ds_read_b128 v[206:209], v168 offset:54272
	ds_read_b128 v[210:213], v168 offset:55296
	ds_read_b128 v[214:217], v168 offset:56320
	global_load_lds_dwordx4 v[162:163], off
	s_add_i32 m0, s30, 0x2000
	s_add_u32 s28, s28, 0x40080
	v_lshl_add_u64 v[162:163], v[202:203], 0, s[78:79]
	s_addc_u32 s29, s29, 0
	s_add_i32 s30, s68, s40
	global_load_lds_dwordx4 v[162:163], off
	v_lshl_add_u64 v[162:163], s[28:29], 0, v[0:1]
	s_mov_b32 m0, s30
	s_nop 0
	global_load_lds_dwordx4 v[162:163], off
	v_lshl_add_u64 v[162:163], s[28:29], 0, v[146:147]
	s_add_i32 m0, s30, 0x2000
	s_nop 0
	global_load_lds_dwordx4 v[162:163], off
	v_lshl_add_u64 v[162:163], v[218:219], 0, s[78:79]
	s_mov_b32 m0, s58
	s_nop 0
	global_load_lds_dwordx4 v[162:163], off
	v_lshl_add_u64 v[162:163], v[222:223], 0, s[78:79]
	s_mov_b32 m0, s61
	s_nop 0
	global_load_lds_dwordx4 v[162:163], off
	s_waitcnt vmcnt(8)
	s_waitcnt lgkmcnt(0)
	s_barrier
	s_setprio 1
	s_waitcnt lgkmcnt(0)
	v_mfma_f32_16x16x32_bf16 v[62:65], v[98:101], v[182:185], v[62:65]
	v_mfma_f32_16x16x32_bf16 v[58:61], v[114:117], v[182:185], v[58:61]
	v_mfma_f32_16x16x32_bf16 v[46:49], v[98:101], v[190:193], v[46:49]
	v_mfma_f32_16x16x32_bf16 v[42:45], v[114:117], v[190:193], v[42:45]
	v_mfma_f32_16x16x32_bf16 v[30:33], v[98:101], v[198:201], v[30:33]
	v_mfma_f32_16x16x32_bf16 v[26:29], v[114:117], v[198:201], v[26:29]
	v_mfma_f32_16x16x32_bf16 v[14:17], v[98:101], v[210:213], v[14:17]
	v_mfma_f32_16x16x32_bf16 v[10:13], v[114:117], v[210:213], v[10:13]
	v_mfma_f32_16x16x32_bf16 v[62:65], v[102:105], v[186:189], v[62:65]
	v_mfma_f32_16x16x32_bf16 v[58:61], v[118:121], v[186:189], v[58:61]
	v_mfma_f32_16x16x32_bf16 v[46:49], v[102:105], v[194:197], v[46:49]
	v_mfma_f32_16x16x32_bf16 v[42:45], v[118:121], v[194:197], v[42:45]
	v_mfma_f32_16x16x32_bf16 v[30:33], v[102:105], v[206:209], v[30:33]
	v_mfma_f32_16x16x32_bf16 v[26:29], v[118:121], v[206:209], v[26:29]
	v_mfma_f32_16x16x32_bf16 v[14:17], v[102:105], v[214:217], v[14:17]
	v_mfma_f32_16x16x32_bf16 v[10:13], v[118:121], v[214:217], v[10:13]
	s_setprio 0
	s_setprio 1
	v_mfma_f32_16x16x32_bf16 v[54:57], v[158:161], v[182:185], v[54:57]
	v_mfma_f32_16x16x32_bf16 v[50:53], v[174:177], v[182:185], v[50:53]
	v_mfma_f32_16x16x32_bf16 v[38:41], v[158:161], v[190:193], v[38:41]
	v_mfma_f32_16x16x32_bf16 v[34:37], v[174:177], v[190:193], v[34:37]
	v_mfma_f32_16x16x32_bf16 v[22:25], v[158:161], v[198:201], v[22:25]
	v_mfma_f32_16x16x32_bf16 v[18:21], v[174:177], v[198:201], v[18:21]
	v_mfma_f32_16x16x32_bf16 v[6:9], v[158:161], v[210:213], v[6:9]
	v_mfma_f32_16x16x32_bf16 v[2:5], v[174:177], v[210:213], v[2:5]
	v_mfma_f32_16x16x32_bf16 v[54:57], v[170:173], v[186:189], v[54:57]
	v_mfma_f32_16x16x32_bf16 v[50:53], v[178:181], v[186:189], v[50:53]
	v_mfma_f32_16x16x32_bf16 v[38:41], v[170:173], v[194:197], v[38:41]
	v_mfma_f32_16x16x32_bf16 v[34:37], v[178:181], v[194:197], v[34:37]
	v_mfma_f32_16x16x32_bf16 v[22:25], v[170:173], v[206:209], v[22:25]
	v_mfma_f32_16x16x32_bf16 v[18:21], v[178:181], v[206:209], v[18:21]
	v_mfma_f32_16x16x32_bf16 v[6:9], v[170:173], v[214:217], v[6:9]
	v_mfma_f32_16x16x32_bf16 v[2:5], v[178:181], v[214:217], v[2:5]
	s_setprio 0
	s_barrier
	s_add_i32 s67, s67, 2
	s_add_u32 s26, s26, 0x100
	s_addc_u32 s27, s27, 0
	s_add_u32 s21, s21, 0x100
	s_addc_u32 s49, s49, 0
	s_cmp_gt_u32 s67, 13

.LBB0_1388:
	s_ashr_i32 s21, s20, 31
	s_lshl_b64 s[24:25], s[20:21], 19
	s_add_u32 s24, s45, s24
	s_addc_u32 s25, s46, s25
	s_and_b64 s[34:35], s[34:35], exec
	s_cselect_b32 s19, s25, s31
	s_cselect_b32 s21, s24, s30
	s_add_u32 s28, s28, 0x40080
	s_addc_u32 s29, s29, 0
	s_add_u32 s49, s30, 0x100
	s_addc_u32 s76, s31, 0
	s_mov_b32 s77, -2
	s_add_u32 s30, s28, 0xfffc0080
	s_addc_u32 s31, s29, -1
	s_cmp_eq_u32 s77, 12
	s_cselect_b32 s35, s23, s31
	s_cselect_b32 s34, s22, s30
	s_cselect_b32 s31, s19, s76
	s_cselect_b32 s30, s21, s49
	s_add_i32 s55, 0, 0x10000
	s_add_i32 s83, 0, 0x14000
	v_add_u32_e32 v142, s55, v230
	v_add_u32_e32 v158, s83, v230
	ds_read_b128 v[130:133], v142
	ds_read_b128 v[134:137], v142 offset:1024
	ds_read_b128 v[138:141], v142 offset:2048
	ds_read_b128 v[142:145], v142 offset:3072
	ds_read_b128 v[146:149], v158
	ds_read_b128 v[150:153], v158 offset:1024
	ds_read_b128 v[154:157], v158 offset:2048
	ds_read_b128 v[158:161], v158 offset:3072
	v_lshl_add_u64 v[216:217], s[28:29], 0, v[202:203]
	s_add_i32 m0, s54, 0xc000
	ds_read_b128 v[162:165], v232
	ds_read_b128 v[166:169], v232 offset:1024
	ds_read_b128 v[170:173], v232 offset:2048
	ds_read_b128 v[174:177], v232 offset:3072
	ds_read_b128 v[178:181], v232 offset:4096
	ds_read_b128 v[182:185], v232 offset:5120
	ds_read_b128 v[208:211], v232 offset:6144
	ds_read_b128 v[212:215], v232 offset:7168
	global_load_lds_dwordx4 v[216:217], off
	v_lshl_add_u64 v[216:217], s[28:29], 0, v[206:207]
	s_add_i32 m0, s54, 0xe000
	s_nop 0
	global_load_lds_dwordx4 v[216:217], off
	s_waitcnt vmcnt(8)
	s_waitcnt lgkmcnt(0)
	s_barrier
	s_setprio 1
	s_waitcnt lgkmcnt(0)
	v_mfma_f32_16x16x32_bf16 v[126:129], v[130:133], v[162:165], 0
	v_mfma_f32_16x16x32_bf16 v[122:125], v[138:141], v[162:165], 0
	v_mfma_f32_16x16x32_bf16 v[110:113], v[130:133], v[170:173], 0
	v_mfma_f32_16x16x32_bf16 v[106:109], v[138:141], v[170:173], 0
	v_mfma_f32_16x16x32_bf16 v[94:97], v[130:133], v[178:181], 0
	v_mfma_f32_16x16x32_bf16 v[90:93], v[138:141], v[178:181], 0
	v_mfma_f32_16x16x32_bf16 v[78:81], v[130:133], v[208:211], 0
	v_mfma_f32_16x16x32_bf16 v[74:77], v[138:141], v[208:211], 0
	v_mfma_f32_16x16x32_bf16 v[126:129], v[134:137], v[166:169], v[126:129]
	v_mfma_f32_16x16x32_bf16 v[122:125], v[142:145], v[166:169], v[122:125]
	v_mfma_f32_16x16x32_bf16 v[110:113], v[134:137], v[174:177], v[110:113]
	v_mfma_f32_16x16x32_bf16 v[106:109], v[142:145], v[174:177], v[106:109]
	v_mfma_f32_16x16x32_bf16 v[94:97], v[134:137], v[182:185], v[94:97]
	v_mfma_f32_16x16x32_bf16 v[90:93], v[142:145], v[182:185], v[90:93]
	v_mfma_f32_16x16x32_bf16 v[78:81], v[134:137], v[212:215], v[78:81]
	v_mfma_f32_16x16x32_bf16 v[74:77], v[142:145], v[212:215], v[74:77]
	s_setprio 0
	s_setprio 1
	v_mfma_f32_16x16x32_bf16 v[118:121], v[146:149], v[162:165], 0
	v_mfma_f32_16x16x32_bf16 v[114:117], v[154:157], v[162:165], 0
	v_mfma_f32_16x16x32_bf16 v[102:105], v[146:149], v[170:173], 0
	v_mfma_f32_16x16x32_bf16 v[98:101], v[154:157], v[170:173], 0
	v_mfma_f32_16x16x32_bf16 v[86:89], v[146:149], v[178:181], 0
	v_mfma_f32_16x16x32_bf16 v[82:85], v[154:157], v[178:181], 0
	v_mfma_f32_16x16x32_bf16 v[70:73], v[146:149], v[208:211], 0
	v_mfma_f32_16x16x32_bf16 v[66:69], v[154:157], v[208:211], 0
	v_mfma_f32_16x16x32_bf16 v[118:121], v[150:153], v[166:169], v[118:121]
	v_mfma_f32_16x16x32_bf16 v[114:117], v[158:161], v[166:169], v[114:117]
	v_mfma_f32_16x16x32_bf16 v[102:105], v[150:153], v[174:177], v[102:105]
	v_mfma_f32_16x16x32_bf16 v[98:101], v[158:161], v[174:177], v[98:101]
	v_mfma_f32_16x16x32_bf16 v[86:89], v[150:153], v[182:185], v[86:89]
	v_mfma_f32_16x16x32_bf16 v[82:85], v[158:161], v[182:185], v[82:85]
	v_mfma_f32_16x16x32_bf16 v[70:73], v[150:153], v[212:215], v[70:73]
	v_mfma_f32_16x16x32_bf16 v[66:69], v[158:161], v[212:215], v[66:69]
	s_setprio 0
	s_barrier
	s_add_i32 s55, s55, s42
	v_lshl_add_u64 v[216:217], s[30:31], 0, v[0:1]
	s_mov_b32 m0, s55
	ds_read_b128 v[162:165], v232 offset:16384
	ds_read_b128 v[166:169], v232 offset:17408
	ds_read_b128 v[170:173], v232 offset:18432
	ds_read_b128 v[174:177], v232 offset:19456
	ds_read_b128 v[178:181], v232 offset:20480
	ds_read_b128 v[182:185], v232 offset:21504
	ds_read_b128 v[208:211], v232 offset:22528
	ds_read_b128 v[212:215], v232 offset:23552
	global_load_lds_dwordx4 v[216:217], off
	s_add_i32 m0, s55, 0x2000
	s_add_u32 s84, s30, 0x40000
	v_lshl_add_u64 v[218:219], s[30:31], 0, v[186:187]
	s_addc_u32 s85, s31, 0
	s_add_i32 s55, s83, s42
	global_load_lds_dwordx4 v[218:219], off
	v_lshl_add_u64 v[222:223], s[84:85], 0, v[0:1]
	s_mov_b32 m0, s55
	v_lshl_add_u64 v[224:225], s[34:35], 0, v[190:191]
	global_load_lds_dwordx4 v[222:223], off
	v_lshl_add_u64 v[222:223], s[84:85], 0, v[186:187]
	s_add_i32 m0, s55, 0x2000
	s_nop 0
	global_load_lds_dwordx4 v[222:223], off
	v_lshl_add_u64 v[222:223], s[34:35], 0, v[188:189]
	s_mov_b32 m0, s54
	s_nop 0
	global_load_lds_dwordx4 v[222:223], off
	s_mov_b32 m0, s58
	s_nop 0
	global_load_lds_dwordx4 v[224:225], off
	s_waitcnt vmcnt(8)
	s_waitcnt lgkmcnt(0)
	s_barrier
	s_setprio 1
	s_waitcnt lgkmcnt(0)
	v_mfma_f32_16x16x32_bf16 v[62:65], v[130:133], v[162:165], 0
	v_mfma_f32_16x16x32_bf16 v[58:61], v[138:141], v[162:165], 0
	v_mfma_f32_16x16x32_bf16 v[46:49], v[130:133], v[170:173], 0
	v_mfma_f32_16x16x32_bf16 v[42:45], v[138:141], v[170:173], 0
	v_mfma_f32_16x16x32_bf16 v[30:33], v[130:133], v[178:181], 0
	v_mfma_f32_16x16x32_bf16 v[26:29], v[138:141], v[178:181], 0
	v_mfma_f32_16x16x32_bf16 v[14:17], v[130:133], v[208:211], 0
	v_mfma_f32_16x16x32_bf16 v[10:13], v[138:141], v[208:211], 0
	v_mfma_f32_16x16x32_bf16 v[62:65], v[134:137], v[166:169], v[62:65]
	v_mfma_f32_16x16x32_bf16 v[58:61], v[142:145], v[166:169], v[58:61]
	v_mfma_f32_16x16x32_bf16 v[46:49], v[134:137], v[174:177], v[46:49]
	v_mfma_f32_16x16x32_bf16 v[42:45], v[142:145], v[174:177], v[42:45]
	v_mfma_f32_16x16x32_bf16 v[30:33], v[134:137], v[182:185], v[30:33]
	v_mfma_f32_16x16x32_bf16 v[26:29], v[142:145], v[182:185], v[26:29]
	v_mfma_f32_16x16x32_bf16 v[14:17], v[134:137], v[212:215], v[14:17]
	v_mfma_f32_16x16x32_bf16 v[10:13], v[142:145], v[212:215], v[10:13]
	s_setprio 0
	s_setprio 1
	v_mfma_f32_16x16x32_bf16 v[54:57], v[146:149], v[162:165], 0
	v_mfma_f32_16x16x32_bf16 v[50:53], v[154:157], v[162:165], 0
	v_mfma_f32_16x16x32_bf16 v[38:41], v[146:149], v[170:173], 0
	v_mfma_f32_16x16x32_bf16 v[34:37], v[154:157], v[170:173], 0
	v_mfma_f32_16x16x32_bf16 v[22:25], v[146:149], v[178:181], 0
	v_mfma_f32_16x16x32_bf16 v[18:21], v[154:157], v[178:181], 0
	v_mfma_f32_16x16x32_bf16 v[6:9], v[146:149], v[208:211], 0
	v_mfma_f32_16x16x32_bf16 v[2:5], v[154:157], v[208:211], 0
	v_mfma_f32_16x16x32_bf16 v[54:57], v[150:153], v[166:169], v[54:57]
	v_mfma_f32_16x16x32_bf16 v[50:53], v[158:161], v[166:169], v[50:53]
	v_mfma_f32_16x16x32_bf16 v[38:41], v[150:153], v[174:177], v[38:41]
	v_mfma_f32_16x16x32_bf16 v[34:37], v[158:161], v[174:177], v[34:37]
	v_mfma_f32_16x16x32_bf16 v[22:25], v[150:153], v[182:185], v[22:25]
	v_mfma_f32_16x16x32_bf16 v[18:21], v[158:161], v[182:185], v[18:21]
	v_mfma_f32_16x16x32_bf16 v[6:9], v[150:153], v[212:215], v[6:9]
	v_mfma_f32_16x16x32_bf16 v[2:5], v[158:161], v[212:215], v[2:5]
	s_setprio 0
	s_barrier
	s_add_i32 s55, 0, 0x18000
	s_add_i32 s83, 0, 0x1c000
	v_add_u32_e32 v142, s55, v230
	v_add_u32_e32 v158, s83, v230
	ds_read_b128 v[130:133], v142
	ds_read_b128 v[134:137], v142 offset:1024
	ds_read_b128 v[138:141], v142 offset:2048
	ds_read_b128 v[142:145], v142 offset:3072
	ds_read_b128 v[146:149], v158
	ds_read_b128 v[150:153], v158 offset:1024
	ds_read_b128 v[154:157], v158 offset:2048
	ds_read_b128 v[158:161], v158 offset:3072
	s_add_u32 s34, s34, 0x40000
	s_addc_u32 s35, s35, 0
	s_mov_b32 m0, s61
	v_lshl_add_u64 v[226:227], s[34:35], 0, v[188:189]
	ds_read_b128 v[162:165], v232 offset:32768
	ds_read_b128 v[166:169], v232 offset:33792
	ds_read_b128 v[170:173], v232 offset:34816
	ds_read_b128 v[174:177], v232 offset:35840
	ds_read_b128 v[178:181], v232 offset:36864
	ds_read_b128 v[182:185], v232 offset:37888
	ds_read_b128 v[208:211], v232 offset:38912
	ds_read_b128 v[212:215], v232 offset:39936
	global_load_lds_dwordx4 v[226:227], off
	v_lshl_add_u64 v[226:227], s[34:35], 0, v[190:191]
	s_mov_b32 m0, s62
	s_nop 0
	global_load_lds_dwordx4 v[226:227], off
	s_waitcnt vmcnt(8)
	s_waitcnt lgkmcnt(0)
	s_barrier
	s_setprio 1
	s_waitcnt lgkmcnt(0)
	v_mfma_f32_16x16x32_bf16 v[126:129], v[130:133], v[162:165], v[126:129]
	v_mfma_f32_16x16x32_bf16 v[122:125], v[138:141], v[162:165], v[122:125]
	v_mfma_f32_16x16x32_bf16 v[110:113], v[130:133], v[170:173], v[110:113]
	v_mfma_f32_16x16x32_bf16 v[106:109], v[138:141], v[170:173], v[106:109]
	v_mfma_f32_16x16x32_bf16 v[94:97], v[130:133], v[178:181], v[94:97]
	v_mfma_f32_16x16x32_bf16 v[90:93], v[138:141], v[178:181], v[90:93]
	v_mfma_f32_16x16x32_bf16 v[78:81], v[130:133], v[208:211], v[78:81]
	v_mfma_f32_16x16x32_bf16 v[74:77], v[138:141], v[208:211], v[74:77]
	v_mfma_f32_16x16x32_bf16 v[126:129], v[134:137], v[166:169], v[126:129]
	v_mfma_f32_16x16x32_bf16 v[122:125], v[142:145], v[166:169], v[122:125]
	v_mfma_f32_16x16x32_bf16 v[110:113], v[134:137], v[174:177], v[110:113]
	v_mfma_f32_16x16x32_bf16 v[106:109], v[142:145], v[174:177], v[106:109]
	v_mfma_f32_16x16x32_bf16 v[94:97], v[134:137], v[182:185], v[94:97]
	v_mfma_f32_16x16x32_bf16 v[90:93], v[142:145], v[182:185], v[90:93]
	v_mfma_f32_16x16x32_bf16 v[78:81], v[134:137], v[212:215], v[78:81]
	v_mfma_f32_16x16x32_bf16 v[74:77], v[142:145], v[212:215], v[74:77]
	s_setprio 0
	s_setprio 1
	v_mfma_f32_16x16x32_bf16 v[118:121], v[146:149], v[162:165], v[118:121]
	v_mfma_f32_16x16x32_bf16 v[114:117], v[154:157], v[162:165], v[114:117]
	v_mfma_f32_16x16x32_bf16 v[102:105], v[146:149], v[170:173], v[102:105]
	v_mfma_f32_16x16x32_bf16 v[98:101], v[154:157], v[170:173], v[98:101]
	v_mfma_f32_16x16x32_bf16 v[86:89], v[146:149], v[178:181], v[86:89]
	v_mfma_f32_16x16x32_bf16 v[82:85], v[154:157], v[178:181], v[82:85]
	v_mfma_f32_16x16x32_bf16 v[70:73], v[146:149], v[208:211], v[70:73]
	v_mfma_f32_16x16x32_bf16 v[66:69], v[154:157], v[208:211], v[66:69]
	v_mfma_f32_16x16x32_bf16 v[118:121], v[150:153], v[166:169], v[118:121]
	v_mfma_f32_16x16x32_bf16 v[114:117], v[158:161], v[166:169], v[114:117]
	v_mfma_f32_16x16x32_bf16 v[102:105], v[150:153], v[174:177], v[102:105]
	v_mfma_f32_16x16x32_bf16 v[98:101], v[158:161], v[174:177], v[98:101]
	v_mfma_f32_16x16x32_bf16 v[86:89], v[150:153], v[182:185], v[86:89]
	v_mfma_f32_16x16x32_bf16 v[82:85], v[158:161], v[182:185], v[82:85]
	v_mfma_f32_16x16x32_bf16 v[70:73], v[150:153], v[212:215], v[70:73]
	v_mfma_f32_16x16x32_bf16 v[66:69], v[158:161], v[212:215], v[66:69]
	s_setprio 0
	s_barrier
	s_add_i32 s34, s55, s42
	v_lshl_add_u64 v[216:217], v[216:217], 0, s[78:79]
	s_mov_b32 m0, s34
	ds_read_b128 v[162:165], v232 offset:49152
	ds_read_b128 v[166:169], v232 offset:50176
	ds_read_b128 v[170:173], v232 offset:51200
	ds_read_b128 v[174:177], v232 offset:52224
	ds_read_b128 v[178:181], v232 offset:53248
	ds_read_b128 v[182:185], v232 offset:54272
	ds_read_b128 v[208:211], v232 offset:55296
	ds_read_b128 v[212:215], v232 offset:56320
	global_load_lds_dwordx4 v[216:217], off
	s_add_i32 m0, s34, 0x2000
	s_add_u32 s30, s30, 0x40080
	v_lshl_add_u64 v[216:217], v[218:219], 0, s[78:79]
	s_addc_u32 s31, s31, 0
	s_add_i32 s34, s83, s42
	global_load_lds_dwordx4 v[216:217], off
	v_lshl_add_u64 v[216:217], s[30:31], 0, v[0:1]
	s_mov_b32 m0, s34
	s_nop 0
	global_load_lds_dwordx4 v[216:217], off
	v_lshl_add_u64 v[216:217], s[30:31], 0, v[186:187]
	s_add_i32 m0, s34, 0x2000
	s_nop 0
	global_load_lds_dwordx4 v[216:217], off
	v_lshl_add_u64 v[216:217], v[222:223], 0, s[78:79]
	s_mov_b32 m0, s68
	s_nop 0
	global_load_lds_dwordx4 v[216:217], off
	v_lshl_add_u64 v[216:217], v[224:225], 0, s[78:79]
	s_mov_b32 m0, s69
	s_nop 0
	global_load_lds_dwordx4 v[216:217], off
	s_waitcnt vmcnt(8)
	s_waitcnt lgkmcnt(0)
	s_barrier
	s_setprio 1
	s_waitcnt lgkmcnt(0)
	v_mfma_f32_16x16x32_bf16 v[62:65], v[130:133], v[162:165], v[62:65]
	v_mfma_f32_16x16x32_bf16 v[58:61], v[138:141], v[162:165], v[58:61]
	v_mfma_f32_16x16x32_bf16 v[46:49], v[130:133], v[170:173], v[46:49]
	v_mfma_f32_16x16x32_bf16 v[42:45], v[138:141], v[170:173], v[42:45]
	v_mfma_f32_16x16x32_bf16 v[30:33], v[130:133], v[178:181], v[30:33]
	v_mfma_f32_16x16x32_bf16 v[26:29], v[138:141], v[178:181], v[26:29]
	v_mfma_f32_16x16x32_bf16 v[14:17], v[130:133], v[208:211], v[14:17]
	v_mfma_f32_16x16x32_bf16 v[10:13], v[138:141], v[208:211], v[10:13]
	v_mfma_f32_16x16x32_bf16 v[62:65], v[134:137], v[166:169], v[62:65]
	v_mfma_f32_16x16x32_bf16 v[58:61], v[142:145], v[166:169], v[58:61]
	v_mfma_f32_16x16x32_bf16 v[46:49], v[134:137], v[174:177], v[46:49]
	v_mfma_f32_16x16x32_bf16 v[42:45], v[142:145], v[174:177], v[42:45]
	v_mfma_f32_16x16x32_bf16 v[30:33], v[134:137], v[182:185], v[30:33]
	v_mfma_f32_16x16x32_bf16 v[26:29], v[142:145], v[182:185], v[26:29]
	v_mfma_f32_16x16x32_bf16 v[14:17], v[134:137], v[212:215], v[14:17]
	v_mfma_f32_16x16x32_bf16 v[10:13], v[142:145], v[212:215], v[10:13]
	s_setprio 0
	s_setprio 1
	v_mfma_f32_16x16x32_bf16 v[54:57], v[146:149], v[162:165], v[54:57]
	v_mfma_f32_16x16x32_bf16 v[50:53], v[154:157], v[162:165], v[50:53]
	v_mfma_f32_16x16x32_bf16 v[38:41], v[146:149], v[170:173], v[38:41]
	v_mfma_f32_16x16x32_bf16 v[34:37], v[154:157], v[170:173], v[34:37]
	v_mfma_f32_16x16x32_bf16 v[22:25], v[146:149], v[178:181], v[22:25]
	v_mfma_f32_16x16x32_bf16 v[18:21], v[154:157], v[178:181], v[18:21]
	v_mfma_f32_16x16x32_bf16 v[6:9], v[146:149], v[208:211], v[6:9]
	v_mfma_f32_16x16x32_bf16 v[2:5], v[154:157], v[208:211], v[2:5]
	v_mfma_f32_16x16x32_bf16 v[54:57], v[150:153], v[166:169], v[54:57]
	v_mfma_f32_16x16x32_bf16 v[50:53], v[158:161], v[166:169], v[50:53]
	v_mfma_f32_16x16x32_bf16 v[38:41], v[150:153], v[174:177], v[38:41]
	v_mfma_f32_16x16x32_bf16 v[34:37], v[158:161], v[174:177], v[34:37]
	v_mfma_f32_16x16x32_bf16 v[22:25], v[150:153], v[182:185], v[22:25]
	v_mfma_f32_16x16x32_bf16 v[18:21], v[158:161], v[182:185], v[18:21]
	v_mfma_f32_16x16x32_bf16 v[6:9], v[150:153], v[212:215], v[6:9]
	v_mfma_f32_16x16x32_bf16 v[2:5], v[158:161], v[212:215], v[2:5]
	s_setprio 0
	s_barrier
	s_add_i32 s77, s77, 2
	s_add_u32 s28, s28, 0x100
	s_addc_u32 s29, s29, 0
	s_add_u32 s49, s49, 0x100
	s_addc_u32 s76, s76, 0
	s_cmp_gt_u32 s77, 13

.LBB0_1867:
	s_add_i32 s58, s58, 1
	s_mul_i32 s5, s58, s3
	s_add_i32 s5, s5, s87
	s_ashr_i32 s12, s5, 2
	s_cmp_lt_i32 s12, s27
	s_cselect_b64 s[16:17], -1, 0
	s_and_b32 s62, s5, 3
	s_cmp_ge_i32 s12, s27
	s_mov_b32 s61, s4
	s_cbranch_scc1 .LBB0_1869
	s_add_i32 s4, s12, 0
	s_add_i32 s4, s4, 0x20400
	v_mov_b32_e32 v3, s4
	v_mbcnt_lo_u32_b32 v2, -1, 0
	v_mbcnt_hi_u32_b32 v2, -1, v2
	ds_read_u8 v3, v3
	s_add_i32 s4, s61, 0
	s_add_i32 m0, s4, 0x25000
	v_lshlrev_b32_e32 v2, 2, v2
	s_waitcnt lgkmcnt(0)
	v_readfirstlane_b32 s4, v3
	s_mov_b32 s100, s4
	s_lshl_b32 s4, s4, 10
	s_ashr_i32 s5, s4, 31
	s_lshl_b64 s[4:5], s[4:5], 2
	s_add_u32 s4, s34, s4
	s_addc_u32 s5, s35, s5
	s_lshl_b32 s13, s62, 10
	s_add_u32 s4, s4, s13
	s_addc_u32 s5, s5, 0
	v_ashrrev_i32_e32 v3, 31, v2
	v_lshl_add_u64 v[2:3], v[2:3], 2, s[4:5]
	global_load_lds_dwordx4 v[2:3], off
	s_ashr_i32 s13, s12, 31
	s_lshl_b64 s[4:5], s[12:13], 18
	s_add_u32 s14, s28, s4
	s_addc_u32 s15, s29, s5
.LBB0_1869:
	v_cndmask_b32_e64 v2, 0, 1, s[16:17]
	v_cmp_ne_u32_e64 s[4:5], 1, v2
	s_andn2_b64 vcc, exec, s[16:17]
	s_mov_b64 s[16:17], s[20:21]
	s_cbranch_vccnz .LBB0_1871
	s_mov_b32 s16, s100
	s_ashr_i32 s17, s16, 31
	s_lshl_b64 s[16:17], s[16:17], 20
	s_add_u32 s13, s30, s16
	s_addc_u32 s17, s31, s17
	s_lshl_b32 s16, s62, 18
	s_add_u32 s16, s13, s16
	s_addc_u32 s17, s17, 0

	.amdhsa_kernel _Z6hh_fwd4Args
		.amdhsa_group_segment_fixed_size 0
		.amdhsa_private_segment_fixed_size 0
		.amdhsa_kernarg_size 552
		.amdhsa_user_sgpr_count 2
		.amdhsa_user_sgpr_dispatch_ptr 0
		.amdhsa_user_sgpr_queue_ptr 0
		.amdhsa_user_sgpr_kernarg_segment_ptr 1
		.amdhsa_user_sgpr_dispatch_id 0
		.amdhsa_user_sgpr_kernarg_preload_length 0
		.amdhsa_user_sgpr_kernarg_preload_offset 0
		.amdhsa_user_sgpr_private_segment_size 0
		.amdhsa_uses_dynamic_stack 0
		.amdhsa_enable_private_segment 0
		.amdhsa_system_sgpr_workgroup_id_x 1
		.amdhsa_system_sgpr_workgroup_id_y 0
		.amdhsa_system_sgpr_workgroup_id_z 0
		.amdhsa_system_sgpr_workgroup_info 0
		.amdhsa_system_vgpr_workitem_id 0
		.amdhsa_next_free_vgpr 256
		.amdhsa_next_free_sgpr 102
		.amdhsa_accum_offset 256
		.amdhsa_reserve_vcc 1
		.amdhsa_float_round_mode_32 0
		.amdhsa_float_round_mode_16_64 0
		.amdhsa_float_denorm_mode_32 3
		.amdhsa_float_denorm_mode_16_64 3
		.amdhsa_dx10_clamp 1
		.amdhsa_ieee_mode 1
		.amdhsa_fp16_overflow 0
		.amdhsa_tg_split 0
		.amdhsa_exception_fp_ieee_invalid_op 0
		.amdhsa_exception_fp_denorm_src 0
		.amdhsa_exception_fp_ieee_div_zero 0
		.amdhsa_exception_fp_ieee_overflow 0
		.amdhsa_exception_fp_ieee_underflow 0
		.amdhsa_exception_fp_ieee_inexact 0
		.amdhsa_exception_int_div_zero 0
	.end_amdhsa_kernel

amdhsa.kernels:
  - .agpr_count:     0
    .args:
      - .offset:         0
        .size:           296
        .value_kind:     by_value
      - .offset:         296
        .size:           4
        .value_kind:     hidden_block_count_x
      - .offset:         300
        .size:           4
        .value_kind:     hidden_block_count_y
      - .offset:         304
        .size:           4
        .value_kind:     hidden_block_count_z
      - .offset:         308
        .size:           2
        .value_kind:     hidden_group_size_x
      - .offset:         310
        .size:           2
        .value_kind:     hidden_group_size_y
      - .offset:         312
        .size:           2
        .value_kind:     hidden_group_size_z
      - .offset:         314
        .size:           2
        .value_kind:     hidden_remainder_x
      - .offset:         316
        .size:           2
        .value_kind:     hidden_remainder_y
      - .offset:         318
        .size:           2
        .value_kind:     hidden_remainder_z
      - .offset:         336
        .size:           8
        .value_kind:     hidden_global_offset_x
      - .offset:         344
        .size:           8
        .value_kind:     hidden_global_offset_y
      - .offset:         352
        .size:           8
        .value_kind:     hidden_global_offset_z
      - .offset:         360
        .size:           2
        .value_kind:     hidden_grid_dims
      - .offset:         416
        .size:           4
        .value_kind:     hidden_dynamic_lds_size
    .group_segment_fixed_size: 0
    .kernarg_segment_align: 8
    .kernarg_segment_size: 552
    .language:       OpenCL C
    .language_version:
      - 2
      - 0
    .max_flat_workgroup_size: 512
    .name:           _Z6hh_fwd4Args
    .private_segment_fixed_size: 0
    .sgpr_count:     108
    .sgpr_spill_count: 113
    .symbol:         _Z6hh_fwd4Args.kd
    .uniform_work_group_size: 1
    .uses_dynamic_stack: false
    .vgpr_count:     256
    .vgpr_spill_count: 0
    .wavefront_size: 64
